# GEMM phases: per-unit accumulator zeroing with 64 v_mov_b64 instead of 128 v_mov_b32
# speedup vs baseline: 1.0015x; 1.0015x over previous
; template <class Epi, class Sched, bool ALIGN_EPI, bool FP8 = false>
; __device__ __forceinline__ void gemm_phase(PG8_LAS unsigned char* lds, const Gemm g, const Sched& S, const Epi& E, const int wid, const int lane) {
;     ...
;     f32x4 acc[2][2][4][2];
; #pragma unroll
;     for (int a = 0; a < 2; ++a)
; #pragma unroll
;         for (int b = 0; b < 2; ++b)
; #pragma unroll
;             for (int m = 0; m < 4; ++m)
; #pragma unroll
;                 for (int n = 0; n < 2; ++n) acc[a][b][m][n] = (f32x4){0.f, 0.f, 0.f, 0.f};
;     ...
; #pragma unroll
;         for (int a = 0; a < 2; ++a)
; #pragma unroll
;             for (int b = 0; b < 2; ++b)
; #pragma unroll
;                 for (int m = 0; m < 4; ++m)
; #pragma unroll
;                     for (int n = 0; n < 2; ++n) acc[a][b][m][n] = (f32x4){0.f, 0.f, 0.f, 0.f};
.LBB0_222:
	v_mov_b32_e32 v3, 0
	s_andn2_b64 vcc, exec, s[14:15]
	v_mov_b64_e32 v[0:1], 0
	v_mov_b64_e32 v[2:3], 0
	v_mov_b64_e32 v[4:5], 0
	v_mov_b64_e32 v[6:7], 0
	v_mov_b64_e32 v[8:9], 0
	v_mov_b64_e32 v[10:11], 0
	v_mov_b64_e32 v[12:13], 0
	v_mov_b64_e32 v[14:15], 0
	v_mov_b64_e32 v[16:17], 0
	v_mov_b64_e32 v[18:19], 0
	v_mov_b64_e32 v[20:21], 0
	v_mov_b64_e32 v[22:23], 0
	v_mov_b64_e32 v[24:25], 0
	v_mov_b64_e32 v[26:27], 0
	v_mov_b64_e32 v[28:29], 0
	v_mov_b64_e32 v[30:31], 0
	v_mov_b64_e32 v[32:33], 0
	v_mov_b64_e32 v[34:35], 0
	v_mov_b64_e32 v[36:37], 0
	v_mov_b64_e32 v[38:39], 0
	v_mov_b64_e32 v[40:41], 0
	v_mov_b64_e32 v[42:43], 0
	v_mov_b64_e32 v[44:45], 0
	v_mov_b64_e32 v[46:47], 0
	v_mov_b64_e32 v[48:49], 0
	v_mov_b64_e32 v[50:51], 0
	v_mov_b64_e32 v[52:53], 0
	v_mov_b64_e32 v[54:55], 0
	v_mov_b64_e32 v[56:57], 0
	v_mov_b64_e32 v[58:59], 0
	v_mov_b64_e32 v[60:61], 0
	v_mov_b64_e32 v[62:63], 0
	v_mov_b64_e32 v[64:65], 0
	v_mov_b64_e32 v[66:67], 0
	v_mov_b64_e32 v[68:69], 0
	v_mov_b64_e32 v[70:71], 0
	v_mov_b64_e32 v[72:73], 0
	v_mov_b64_e32 v[74:75], 0
	v_mov_b64_e32 v[76:77], 0
	v_mov_b64_e32 v[78:79], 0
	v_mov_b64_e32 v[80:81], 0
	v_mov_b64_e32 v[82:83], 0
	v_mov_b64_e32 v[84:85], 0
	v_mov_b64_e32 v[86:87], 0
	v_mov_b64_e32 v[88:89], 0
	v_mov_b64_e32 v[90:91], 0
	v_mov_b64_e32 v[92:93], 0
	v_mov_b64_e32 v[94:95], 0
	v_mov_b64_e32 v[96:97], 0
	v_mov_b64_e32 v[98:99], 0
	v_mov_b64_e32 v[100:101], 0
	v_mov_b64_e32 v[102:103], 0
	v_mov_b64_e32 v[104:105], 0
	v_mov_b64_e32 v[106:107], 0
	v_mov_b64_e32 v[108:109], 0
	v_mov_b64_e32 v[110:111], 0
	v_mov_b64_e32 v[112:113], 0
	v_mov_b64_e32 v[114:115], 0
	v_mov_b64_e32 v[116:117], 0
	v_mov_b64_e32 v[118:119], 0
	v_mov_b64_e32 v[120:121], 0
	v_mov_b64_e32 v[122:123], 0
	v_mov_b64_e32 v[124:125], 0
	v_mov_b64_e32 v[126:127], 0
	s_cbranch_vccnz .LBB0_225
	s_add_u32 s4, s28, s6
	s_addc_u32 s5, s29, s7
	s_add_u32 s60, s28, 0x100
	s_addc_u32 s61, s29, 0
	s_add_u32 s62, s26, 0x100
	s_addc_u32 s63, s27, 0
	s_add_u32 s4, s4, 0x80
	v_mov_b32_e32 v32, 0
	s_addc_u32 s5, s5, 0
	s_mov_b32 s26, 0
	v_mov_b64_e32 v[0:1], 0
	v_mov_b64_e32 v[2:3], 0
	v_mov_b64_e32 v[4:5], 0
	v_mov_b64_e32 v[6:7], 0
	v_mov_b64_e32 v[8:9], 0
	v_mov_b64_e32 v[10:11], 0
	v_mov_b64_e32 v[12:13], 0
	v_mov_b64_e32 v[14:15], 0
	v_mov_b64_e32 v[16:17], 0
	v_mov_b64_e32 v[18:19], 0
	v_mov_b64_e32 v[20:21], 0
	v_mov_b64_e32 v[22:23], 0
	v_mov_b64_e32 v[24:25], 0
	v_mov_b64_e32 v[26:27], 0
	v_mov_b64_e32 v[28:29], 0
	v_mov_b64_e32 v[30:31], 0
	v_mov_b64_e32 v[32:33], 0
	v_mov_b64_e32 v[34:35], 0
	v_mov_b64_e32 v[36:37], 0
	v_mov_b64_e32 v[38:39], 0
	v_mov_b64_e32 v[40:41], 0
	v_mov_b64_e32 v[42:43], 0
	v_mov_b64_e32 v[44:45], 0
	v_mov_b64_e32 v[46:47], 0
	v_mov_b64_e32 v[48:49], 0
	v_mov_b64_e32 v[50:51], 0
	v_mov_b64_e32 v[52:53], 0
	v_mov_b64_e32 v[54:55], 0
	v_mov_b64_e32 v[56:57], 0
	v_mov_b64_e32 v[58:59], 0
	v_mov_b64_e32 v[60:61], 0
	v_mov_b64_e32 v[62:63], 0
	v_mov_b64_e32 v[64:65], 0
	v_mov_b64_e32 v[66:67], 0
	v_mov_b64_e32 v[68:69], 0
	v_mov_b64_e32 v[70:71], 0
	v_mov_b64_e32 v[72:73], 0
	v_mov_b64_e32 v[74:75], 0
	v_mov_b64_e32 v[76:77], 0
	v_mov_b64_e32 v[78:79], 0
	v_mov_b64_e32 v[80:81], 0
	v_mov_b64_e32 v[82:83], 0
	v_mov_b64_e32 v[84:85], 0
	v_mov_b64_e32 v[86:87], 0
	v_mov_b64_e32 v[88:89], 0
	v_mov_b64_e32 v[90:91], 0
	v_mov_b64_e32 v[92:93], 0
	v_mov_b64_e32 v[94:95], 0
	v_mov_b64_e32 v[96:97], 0
	v_mov_b64_e32 v[98:99], 0
	v_mov_b64_e32 v[100:101], 0
	v_mov_b64_e32 v[102:103], 0
	v_mov_b64_e32 v[104:105], 0
	v_mov_b64_e32 v[106:107], 0
	v_mov_b64_e32 v[108:109], 0
	v_mov_b64_e32 v[110:111], 0
	v_mov_b64_e32 v[112:113], 0
	v_mov_b64_e32 v[114:115], 0
	v_mov_b64_e32 v[116:117], 0
	v_mov_b64_e32 v[118:119], 0
	v_mov_b64_e32 v[120:121], 0
	v_mov_b64_e32 v[122:123], 0
	v_mov_b64_e32 v[124:125], 0
	v_mov_b64_e32 v[126:127], 0

; template <class Epi, class Sched, bool ALIGN_EPI, bool FP8 = false>
; __device__ __forceinline__ void gemm_phase(PG8_LAS unsigned char* lds, const Gemm g, const Sched& S, const Epi& E, const int wid, const int lane) {
;     ...
;     f32x4 acc[2][2][4][2];
; #pragma unroll
;     for (int a = 0; a < 2; ++a)
; #pragma unroll
;         for (int b = 0; b < 2; ++b)
; #pragma unroll
;             for (int m = 0; m < 4; ++m)
; #pragma unroll
;                 for (int n = 0; n < 2; ++n) acc[a][b][m][n] = (f32x4){0.f, 0.f, 0.f, 0.f};
;     ...
; #pragma unroll
;         for (int a = 0; a < 2; ++a)
; #pragma unroll
;             for (int b = 0; b < 2; ++b)
; #pragma unroll
;                 for (int m = 0; m < 4; ++m)
; #pragma unroll
;                     for (int n = 0; n < 2; ++n) acc[a][b][m][n] = (f32x4){0.f, 0.f, 0.f, 0.f};
.LBB0_542:
	v_mov_b32_e32 v35, 0
	s_andn2_b64 vcc, exec, s[14:15]
	v_mov_b64_e32 v[32:33], 0
	v_mov_b64_e32 v[34:35], 0
	v_mov_b64_e32 v[36:37], 0
	v_mov_b64_e32 v[38:39], 0
	v_mov_b64_e32 v[40:41], 0
	v_mov_b64_e32 v[42:43], 0
	v_mov_b64_e32 v[44:45], 0
	v_mov_b64_e32 v[46:47], 0
	v_mov_b64_e32 v[48:49], 0
	v_mov_b64_e32 v[50:51], 0
	v_mov_b64_e32 v[52:53], 0
	v_mov_b64_e32 v[54:55], 0
	v_mov_b64_e32 v[56:57], 0
	v_mov_b64_e32 v[58:59], 0
	v_mov_b64_e32 v[60:61], 0
	v_mov_b64_e32 v[62:63], 0
	v_mov_b64_e32 v[64:65], 0
	v_mov_b64_e32 v[66:67], 0
	v_mov_b64_e32 v[68:69], 0
	v_mov_b64_e32 v[70:71], 0
	v_mov_b64_e32 v[72:73], 0
	v_mov_b64_e32 v[74:75], 0
	v_mov_b64_e32 v[76:77], 0
	v_mov_b64_e32 v[78:79], 0
	v_mov_b64_e32 v[80:81], 0
	v_mov_b64_e32 v[82:83], 0
	v_mov_b64_e32 v[84:85], 0
	v_mov_b64_e32 v[86:87], 0
	v_mov_b64_e32 v[88:89], 0
	v_mov_b64_e32 v[90:91], 0
	v_mov_b64_e32 v[92:93], 0
	v_mov_b64_e32 v[94:95], 0
	v_mov_b64_e32 v[96:97], 0
	v_mov_b64_e32 v[98:99], 0
	v_mov_b64_e32 v[100:101], 0
	v_mov_b64_e32 v[102:103], 0
	v_mov_b64_e32 v[104:105], 0
	v_mov_b64_e32 v[106:107], 0
	v_mov_b64_e32 v[108:109], 0
	v_mov_b64_e32 v[110:111], 0
	v_mov_b64_e32 v[112:113], 0
	v_mov_b64_e32 v[114:115], 0
	v_mov_b64_e32 v[116:117], 0
	v_mov_b64_e32 v[118:119], 0
	v_mov_b64_e32 v[120:121], 0
	v_mov_b64_e32 v[122:123], 0
	v_mov_b64_e32 v[124:125], 0
	v_mov_b64_e32 v[126:127], 0
	v_mov_b64_e32 v[128:129], 0
	v_mov_b64_e32 v[130:131], 0
	v_mov_b64_e32 v[132:133], 0
	v_mov_b64_e32 v[134:135], 0
	v_mov_b64_e32 v[136:137], 0
	v_mov_b64_e32 v[138:139], 0
	v_mov_b64_e32 v[140:141], 0
	v_mov_b64_e32 v[142:143], 0
	v_mov_b64_e32 v[144:145], 0
	v_mov_b64_e32 v[146:147], 0
	v_mov_b64_e32 v[148:149], 0
	v_mov_b64_e32 v[150:151], 0
	v_mov_b64_e32 v[152:153], 0
	v_mov_b64_e32 v[154:155], 0
	v_mov_b64_e32 v[156:157], 0
	v_mov_b64_e32 v[158:159], 0
	s_cbranch_vccnz .LBB0_545
	s_add_u32 s33, s30, s6
	s_addc_u32 s34, s31, s7
	s_add_u32 s82, s30, 0x100
	s_addc_u32 s85, s31, 0
	s_add_u32 s86, s28, 0x100
	s_addc_u32 s87, s29, 0
	s_add_u32 s28, s33, 0x80
	v_mov_b32_e32 v64, 0
	s_addc_u32 s29, s34, 0
	s_mov_b32 s30, 0
	v_mov_b64_e32 v[32:33], 0
	v_mov_b64_e32 v[34:35], 0
	v_mov_b64_e32 v[36:37], 0
	v_mov_b64_e32 v[38:39], 0
	v_mov_b64_e32 v[40:41], 0
	v_mov_b64_e32 v[42:43], 0
	v_mov_b64_e32 v[44:45], 0
	v_mov_b64_e32 v[46:47], 0
	v_mov_b64_e32 v[48:49], 0
	v_mov_b64_e32 v[50:51], 0
	v_mov_b64_e32 v[52:53], 0
	v_mov_b64_e32 v[54:55], 0
	v_mov_b64_e32 v[56:57], 0
	v_mov_b64_e32 v[58:59], 0
	v_mov_b64_e32 v[60:61], 0
	v_mov_b64_e32 v[62:63], 0
	v_mov_b64_e32 v[64:65], 0
	v_mov_b64_e32 v[66:67], 0
	v_mov_b64_e32 v[68:69], 0
	v_mov_b64_e32 v[70:71], 0
	v_mov_b64_e32 v[72:73], 0
	v_mov_b64_e32 v[74:75], 0
	v_mov_b64_e32 v[76:77], 0
	v_mov_b64_e32 v[78:79], 0
	v_mov_b64_e32 v[80:81], 0
	v_mov_b64_e32 v[82:83], 0
	v_mov_b64_e32 v[84:85], 0
	v_mov_b64_e32 v[86:87], 0
	v_mov_b64_e32 v[88:89], 0
	v_mov_b64_e32 v[90:91], 0
	v_mov_b64_e32 v[92:93], 0
	v_mov_b64_e32 v[94:95], 0
	v_mov_b64_e32 v[96:97], 0
	v_mov_b64_e32 v[98:99], 0
	v_mov_b64_e32 v[100:101], 0
	v_mov_b64_e32 v[102:103], 0
	v_mov_b64_e32 v[104:105], 0
	v_mov_b64_e32 v[106:107], 0
	v_mov_b64_e32 v[108:109], 0
	v_mov_b64_e32 v[110:111], 0
	v_mov_b64_e32 v[112:113], 0
	v_mov_b64_e32 v[114:115], 0
	v_mov_b64_e32 v[116:117], 0
	v_mov_b64_e32 v[118:119], 0
	v_mov_b64_e32 v[120:121], 0
	v_mov_b64_e32 v[122:123], 0
	v_mov_b64_e32 v[124:125], 0
	v_mov_b64_e32 v[126:127], 0
	v_mov_b64_e32 v[128:129], 0
	v_mov_b64_e32 v[130:131], 0
	v_mov_b64_e32 v[132:133], 0
	v_mov_b64_e32 v[134:135], 0
	v_mov_b64_e32 v[136:137], 0
	v_mov_b64_e32 v[138:139], 0
	v_mov_b64_e32 v[140:141], 0
	v_mov_b64_e32 v[142:143], 0
	v_mov_b64_e32 v[144:145], 0
	v_mov_b64_e32 v[146:147], 0
	v_mov_b64_e32 v[148:149], 0
	v_mov_b64_e32 v[150:151], 0
	v_mov_b64_e32 v[152:153], 0
	v_mov_b64_e32 v[154:155], 0
	v_mov_b64_e32 v[156:157], 0
	v_mov_b64_e32 v[158:159], 0

; template <class Epi, class Sched, bool ALIGN_EPI, bool FP8 = false>
; __device__ __forceinline__ void gemm_phase(PG8_LAS unsigned char* lds, const Gemm g, const Sched& S, const Epi& E, const int wid, const int lane) {
;     ...
; #pragma unroll
;         for (int a = 0; a < 2; ++a)
; #pragma unroll
;             for (int b = 0; b < 2; ++b)
; #pragma unroll
;                 for (int m = 0; m < 4; ++m)
; #pragma unroll
;                     for (int n = 0; n < 2; ++n) acc[a][b][m][n] = (f32x4){0.f, 0.f, 0.f, 0.f};
.LBB0_726:
	v_mov_b32_e32 v68, 0
	s_mov_b32 s82, 0
	s_mov_b64 s[6:7], 0x100
	v_mov_b64_e32 v[68:69], 0
	v_mov_b64_e32 v[70:71], 0
	v_mov_b64_e32 v[72:73], 0
	v_mov_b64_e32 v[74:75], 0
	v_mov_b64_e32 v[76:77], 0
	v_mov_b64_e32 v[78:79], 0
	v_mov_b64_e32 v[80:81], 0
	v_mov_b64_e32 v[82:83], 0
	v_mov_b64_e32 v[84:85], 0
	v_mov_b64_e32 v[86:87], 0
	v_mov_b64_e32 v[88:89], 0
	v_mov_b64_e32 v[90:91], 0
	v_mov_b64_e32 v[92:93], 0
	v_mov_b64_e32 v[94:95], 0
	v_mov_b64_e32 v[96:97], 0
	v_mov_b64_e32 v[98:99], 0
	v_mov_b64_e32 v[100:101], 0
	v_mov_b64_e32 v[102:103], 0
	v_mov_b64_e32 v[104:105], 0
	v_mov_b64_e32 v[106:107], 0
	v_mov_b64_e32 v[108:109], 0
	v_mov_b64_e32 v[110:111], 0
	v_mov_b64_e32 v[112:113], 0
	v_mov_b64_e32 v[114:115], 0
	v_mov_b64_e32 v[116:117], 0
	v_mov_b64_e32 v[118:119], 0
	v_mov_b64_e32 v[120:121], 0
	v_mov_b64_e32 v[122:123], 0
	v_mov_b64_e32 v[124:125], 0
	v_mov_b64_e32 v[126:127], 0
	v_mov_b64_e32 v[128:129], 0
	v_mov_b64_e32 v[130:131], 0
	v_mov_b64_e32 v[132:133], 0
	v_mov_b64_e32 v[134:135], 0
	v_mov_b64_e32 v[136:137], 0
	v_mov_b64_e32 v[138:139], 0
	v_mov_b64_e32 v[140:141], 0
	v_mov_b64_e32 v[142:143], 0
	v_mov_b64_e32 v[144:145], 0
	v_mov_b64_e32 v[146:147], 0
	v_mov_b64_e32 v[148:149], 0
	v_mov_b64_e32 v[150:151], 0
	v_mov_b64_e32 v[152:153], 0
	v_mov_b64_e32 v[154:155], 0
	v_mov_b64_e32 v[156:157], 0
	v_mov_b64_e32 v[158:159], 0
	v_mov_b64_e32 v[160:161], 0
	v_mov_b64_e32 v[162:163], 0
	v_mov_b64_e32 v[164:165], 0
	v_mov_b64_e32 v[166:167], 0
	v_mov_b64_e32 v[168:169], 0
	v_mov_b64_e32 v[170:171], 0
	v_mov_b64_e32 v[172:173], 0
	v_mov_b64_e32 v[174:175], 0
	v_mov_b64_e32 v[176:177], 0
	v_mov_b64_e32 v[178:179], 0
	v_mov_b64_e32 v[180:181], 0
	v_mov_b64_e32 v[182:183], 0
	v_mov_b64_e32 v[184:185], 0
	v_mov_b64_e32 v[186:187], 0
	v_mov_b64_e32 v[188:189], 0
	v_mov_b64_e32 v[190:191], 0
	v_mov_b64_e32 v[192:193], 0
	v_mov_b64_e32 v[194:195], 0
	s_branch .LBB0_728

; template <class Epi, class Sched, bool ALIGN_EPI, bool FP8 = false>
; __device__ __forceinline__ void gemm_phase(PG8_LAS unsigned char* lds, const Gemm g, const Sched& S, const Epi& E, const int wid, const int lane) {
;     ...
;     f32x4 acc[2][2][4][2];
; #pragma unroll
;     for (int a = 0; a < 2; ++a)
; #pragma unroll
;         for (int b = 0; b < 2; ++b)
; #pragma unroll
;             for (int m = 0; m < 4; ++m)
; #pragma unroll
;                 for (int n = 0; n < 2; ++n) acc[a][b][m][n] = (f32x4){0.f, 0.f, 0.f, 0.f};
;     ...
; #pragma unroll
;         for (int a = 0; a < 2; ++a)
; #pragma unroll
;             for (int b = 0; b < 2; ++b)
; #pragma unroll
;                 for (int m = 0; m < 4; ++m)
; #pragma unroll
;                     for (int n = 0; n < 2; ++n) acc[a][b][m][n] = (f32x4){0.f, 0.f, 0.f, 0.f};
.LBB0_748:
	v_mov_b64_e32 v[68:69], 0
	v_mov_b64_e32 v[70:71], 0
	v_mov_b64_e32 v[72:73], 0
	v_mov_b64_e32 v[74:75], 0
	v_mov_b64_e32 v[76:77], 0
	v_mov_b64_e32 v[78:79], 0
	v_mov_b64_e32 v[80:81], 0
	v_mov_b64_e32 v[82:83], 0
	v_mov_b64_e32 v[84:85], 0
	v_mov_b64_e32 v[86:87], 0
	v_mov_b64_e32 v[88:89], 0
	v_mov_b64_e32 v[90:91], 0
	v_mov_b64_e32 v[92:93], 0
	v_mov_b64_e32 v[94:95], 0
	v_mov_b64_e32 v[96:97], 0
	v_mov_b64_e32 v[98:99], 0
	v_mov_b64_e32 v[100:101], 0
	v_mov_b64_e32 v[102:103], 0
	v_mov_b64_e32 v[104:105], 0
	v_mov_b64_e32 v[106:107], 0
	v_mov_b64_e32 v[108:109], 0
	v_mov_b64_e32 v[110:111], 0
	v_mov_b64_e32 v[112:113], 0
	v_mov_b64_e32 v[114:115], 0
	v_mov_b64_e32 v[116:117], 0
	v_mov_b64_e32 v[118:119], 0
	v_mov_b64_e32 v[120:121], 0
	v_mov_b64_e32 v[122:123], 0
	v_mov_b64_e32 v[124:125], 0
	v_mov_b64_e32 v[126:127], 0
	v_mov_b64_e32 v[128:129], 0
	v_mov_b64_e32 v[130:131], 0
	v_mov_b64_e32 v[132:133], 0
	v_mov_b64_e32 v[134:135], 0
	v_mov_b64_e32 v[136:137], 0
	v_mov_b64_e32 v[138:139], 0
	v_mov_b64_e32 v[140:141], 0
	v_mov_b64_e32 v[142:143], 0
	v_mov_b64_e32 v[144:145], 0
	v_mov_b64_e32 v[146:147], 0
	v_mov_b64_e32 v[148:149], 0
	v_mov_b64_e32 v[150:151], 0
	v_mov_b64_e32 v[152:153], 0
	v_mov_b64_e32 v[154:155], 0
	v_mov_b64_e32 v[156:157], 0
	v_mov_b64_e32 v[158:159], 0
	v_mov_b64_e32 v[160:161], 0
	v_mov_b64_e32 v[162:163], 0
	v_mov_b64_e32 v[164:165], 0
	v_mov_b64_e32 v[166:167], 0
	v_mov_b64_e32 v[168:169], 0
	v_mov_b64_e32 v[170:171], 0
	v_mov_b64_e32 v[172:173], 0
	v_mov_b64_e32 v[174:175], 0
	v_mov_b64_e32 v[176:177], 0
	v_mov_b64_e32 v[178:179], 0
	v_mov_b64_e32 v[180:181], 0
	v_mov_b64_e32 v[182:183], 0
	v_mov_b64_e32 v[184:185], 0
	v_mov_b64_e32 v[186:187], 0
	v_mov_b64_e32 v[188:189], 0
	v_mov_b64_e32 v[190:191], 0
	v_mov_b64_e32 v[192:193], 0
	v_mov_b64_e32 v[194:195], 0

; template <class Epi, class Sched, bool ALIGN_EPI, bool FP8 = false>
; __device__ __forceinline__ void gemm_phase(PG8_LAS unsigned char* lds, const Gemm g, const Sched& S, const Epi& E, const int wid, const int lane) {
;     ...
;     f32x4 acc[2][2][4][2];
; #pragma unroll
;     for (int a = 0; a < 2; ++a)
; #pragma unroll
;         for (int b = 0; b < 2; ++b)
; #pragma unroll
;             for (int m = 0; m < 4; ++m)
; #pragma unroll
;                 for (int n = 0; n < 2; ++n) acc[a][b][m][n] = (f32x4){0.f, 0.f, 0.f, 0.f};
;     ...
; #pragma unroll
;         for (int a = 0; a < 2; ++a)
; #pragma unroll
;             for (int b = 0; b < 2; ++b)
; #pragma unroll
;                 for (int m = 0; m < 4; ++m)
; #pragma unroll
;                     for (int n = 0; n < 2; ++n) acc[a][b][m][n] = (f32x4){0.f, 0.f, 0.f, 0.f};
.LBB0_850:
	v_mov_b32_e32 v35, 0
	s_andn2_b64 vcc, exec, s[22:23]
	v_mov_b64_e32 v[32:33], 0
	v_mov_b64_e32 v[34:35], 0
	v_mov_b64_e32 v[36:37], 0
	v_mov_b64_e32 v[38:39], 0
	v_mov_b64_e32 v[40:41], 0
	v_mov_b64_e32 v[42:43], 0
	v_mov_b64_e32 v[44:45], 0
	v_mov_b64_e32 v[46:47], 0
	v_mov_b64_e32 v[48:49], 0
	v_mov_b64_e32 v[50:51], 0
	v_mov_b64_e32 v[52:53], 0
	v_mov_b64_e32 v[54:55], 0
	v_mov_b64_e32 v[56:57], 0
	v_mov_b64_e32 v[58:59], 0
	v_mov_b64_e32 v[60:61], 0
	v_mov_b64_e32 v[62:63], 0
	v_mov_b64_e32 v[64:65], 0
	v_mov_b64_e32 v[66:67], 0
	v_mov_b64_e32 v[68:69], 0
	v_mov_b64_e32 v[70:71], 0
	v_mov_b64_e32 v[72:73], 0
	v_mov_b64_e32 v[74:75], 0
	v_mov_b64_e32 v[76:77], 0
	v_mov_b64_e32 v[78:79], 0
	v_mov_b64_e32 v[80:81], 0
	v_mov_b64_e32 v[82:83], 0
	v_mov_b64_e32 v[84:85], 0
	v_mov_b64_e32 v[86:87], 0
	v_mov_b64_e32 v[88:89], 0
	v_mov_b64_e32 v[90:91], 0
	v_mov_b64_e32 v[92:93], 0
	v_mov_b64_e32 v[94:95], 0
	v_mov_b64_e32 v[96:97], 0
	v_mov_b64_e32 v[98:99], 0
	v_mov_b64_e32 v[100:101], 0
	v_mov_b64_e32 v[102:103], 0
	v_mov_b64_e32 v[104:105], 0
	v_mov_b64_e32 v[106:107], 0
	v_mov_b64_e32 v[108:109], 0
	v_mov_b64_e32 v[110:111], 0
	v_mov_b64_e32 v[112:113], 0
	v_mov_b64_e32 v[114:115], 0
	v_mov_b64_e32 v[116:117], 0
	v_mov_b64_e32 v[118:119], 0
	v_mov_b64_e32 v[120:121], 0
	v_mov_b64_e32 v[122:123], 0
	v_mov_b64_e32 v[124:125], 0
	v_mov_b64_e32 v[126:127], 0
	v_mov_b64_e32 v[128:129], 0
	v_mov_b64_e32 v[130:131], 0
	v_mov_b64_e32 v[132:133], 0
	v_mov_b64_e32 v[134:135], 0
	v_mov_b64_e32 v[136:137], 0
	v_mov_b64_e32 v[138:139], 0
	v_mov_b64_e32 v[140:141], 0
	v_mov_b64_e32 v[142:143], 0
	v_mov_b64_e32 v[144:145], 0
	v_mov_b64_e32 v[146:147], 0
	v_mov_b64_e32 v[148:149], 0
	v_mov_b64_e32 v[150:151], 0
	v_mov_b64_e32 v[152:153], 0
	v_mov_b64_e32 v[154:155], 0
	v_mov_b64_e32 v[156:157], 0
	v_mov_b64_e32 v[158:159], 0
	s_cbranch_vccnz .LBB0_853
	s_add_u32 s33, s8, s12
	s_addc_u32 s34, s9, s13
	s_add_u32 s75, s8, 0x100
	s_addc_u32 s82, s9, 0
	s_add_u32 s83, s6, 0x100
	s_addc_u32 s84, s7, 0
	s_add_u32 s6, s33, 0x80
	v_mov_b32_e32 v64, 0
	s_addc_u32 s7, s34, 0
	s_mov_b32 s8, 0
	v_mov_b64_e32 v[32:33], 0
	v_mov_b64_e32 v[34:35], 0
	v_mov_b64_e32 v[36:37], 0
	v_mov_b64_e32 v[38:39], 0
	v_mov_b64_e32 v[40:41], 0
	v_mov_b64_e32 v[42:43], 0
	v_mov_b64_e32 v[44:45], 0
	v_mov_b64_e32 v[46:47], 0
	v_mov_b64_e32 v[48:49], 0
	v_mov_b64_e32 v[50:51], 0
	v_mov_b64_e32 v[52:53], 0
	v_mov_b64_e32 v[54:55], 0
	v_mov_b64_e32 v[56:57], 0
	v_mov_b64_e32 v[58:59], 0
	v_mov_b64_e32 v[60:61], 0
	v_mov_b64_e32 v[62:63], 0
	v_mov_b64_e32 v[64:65], 0
	v_mov_b64_e32 v[66:67], 0
	v_mov_b64_e32 v[68:69], 0
	v_mov_b64_e32 v[70:71], 0
	v_mov_b64_e32 v[72:73], 0
	v_mov_b64_e32 v[74:75], 0
	v_mov_b64_e32 v[76:77], 0
	v_mov_b64_e32 v[78:79], 0
	v_mov_b64_e32 v[80:81], 0
	v_mov_b64_e32 v[82:83], 0
	v_mov_b64_e32 v[84:85], 0
	v_mov_b64_e32 v[86:87], 0
	v_mov_b64_e32 v[88:89], 0
	v_mov_b64_e32 v[90:91], 0
	v_mov_b64_e32 v[92:93], 0
	v_mov_b64_e32 v[94:95], 0
	v_mov_b64_e32 v[96:97], 0
	v_mov_b64_e32 v[98:99], 0
	v_mov_b64_e32 v[100:101], 0
	v_mov_b64_e32 v[102:103], 0
	v_mov_b64_e32 v[104:105], 0
	v_mov_b64_e32 v[106:107], 0
	v_mov_b64_e32 v[108:109], 0
	v_mov_b64_e32 v[110:111], 0
	v_mov_b64_e32 v[112:113], 0
	v_mov_b64_e32 v[114:115], 0
	v_mov_b64_e32 v[116:117], 0
	v_mov_b64_e32 v[118:119], 0
	v_mov_b64_e32 v[120:121], 0
	v_mov_b64_e32 v[122:123], 0
	v_mov_b64_e32 v[124:125], 0
	v_mov_b64_e32 v[126:127], 0
	v_mov_b64_e32 v[128:129], 0
	v_mov_b64_e32 v[130:131], 0
	v_mov_b64_e32 v[132:133], 0
	v_mov_b64_e32 v[134:135], 0
	v_mov_b64_e32 v[136:137], 0
	v_mov_b64_e32 v[138:139], 0
	v_mov_b64_e32 v[140:141], 0
	v_mov_b64_e32 v[142:143], 0
	v_mov_b64_e32 v[144:145], 0
	v_mov_b64_e32 v[146:147], 0
	v_mov_b64_e32 v[148:149], 0
	v_mov_b64_e32 v[150:151], 0
	v_mov_b64_e32 v[152:153], 0
	v_mov_b64_e32 v[154:155], 0
	v_mov_b64_e32 v[156:157], 0
	v_mov_b64_e32 v[158:159], 0

; template <class Epi, class Sched, bool ALIGN_EPI, bool FP8 = false>
; __device__ __forceinline__ void gemm_phase(PG8_LAS unsigned char* lds, const Gemm g, const Sched& S, const Epi& E, const int wid, const int lane) {
;     ...
;     f32x4 acc[2][2][4][2];
; #pragma unroll
;     for (int a = 0; a < 2; ++a)
; #pragma unroll
;         for (int b = 0; b < 2; ++b)
; #pragma unroll
;             for (int m = 0; m < 4; ++m)
; #pragma unroll
;                 for (int n = 0; n < 2; ++n) acc[a][b][m][n] = (f32x4){0.f, 0.f, 0.f, 0.f};
;     ...
; #pragma unroll
;         for (int a = 0; a < 2; ++a)
; #pragma unroll
;             for (int b = 0; b < 2; ++b)
; #pragma unroll
;                 for (int m = 0; m < 4; ++m)
; #pragma unroll
;                     for (int n = 0; n < 2; ++n) acc[a][b][m][n] = (f32x4){0.f, 0.f, 0.f, 0.f};
.LBB0_1132:
	v_mov_b32_e32 v3, 0
	s_andn2_b64 vcc, exec, s[14:15]
	v_mov_b32_e32 v2, v3
	v_mov_b32_e32 v1, v3
	v_mov_b32_e32 v0, v3
	v_mov_b32_e32 v7, v3
	v_mov_b32_e32 v6, v3
	v_mov_b32_e32 v5, v3
	v_mov_b32_e32 v4, v3
	s_waitcnt vmcnt(13)
	v_mov_b32_e32 v19, v3
	v_mov_b32_e32 v18, v3
	v_mov_b32_e32 v17, v3
	v_mov_b32_e32 v16, v3
	s_waitcnt vmcnt(12)
	v_mov_b32_e32 v23, v3
	v_mov_b32_e32 v22, v3
	v_mov_b32_e32 v21, v3
	v_mov_b32_e32 v20, v3
	v_mov_b32_e32 v127, v3
	v_mov_b32_e32 v126, v3
	v_mov_b32_e32 v125, v3
	v_mov_b32_e32 v124, v3
	v_mov_b32_e32 v123, v3
	v_mov_b32_e32 v122, v3
	v_mov_b32_e32 v121, v3
	v_mov_b32_e32 v120, v3
	v_mov_b32_e32 v111, v3
	v_mov_b32_e32 v110, v3
	v_mov_b32_e32 v109, v3
	v_mov_b32_e32 v108, v3
	v_mov_b32_e32 v107, v3
	v_mov_b32_e32 v106, v3
	v_mov_b32_e32 v105, v3
	v_mov_b32_e32 v104, v3
	v_mov_b32_e32 v95, v3
	v_mov_b32_e32 v94, v3
	v_mov_b32_e32 v93, v3
	v_mov_b32_e32 v92, v3
	v_mov_b32_e32 v91, v3
	v_mov_b32_e32 v90, v3
	v_mov_b32_e32 v89, v3
	v_mov_b32_e32 v88, v3
	s_waitcnt vmcnt(0)
	v_mov_b64_e32 v[8:9], 0
	v_mov_b64_e32 v[10:11], 0
	v_mov_b64_e32 v[12:13], 0
	v_mov_b64_e32 v[14:15], 0
	v_mov_b64_e32 v[24:25], 0
	v_mov_b64_e32 v[26:27], 0
	v_mov_b64_e32 v[28:29], 0
	v_mov_b64_e32 v[30:31], 0
	v_mov_b64_e32 v[32:33], 0
	v_mov_b64_e32 v[34:35], 0
	v_mov_b64_e32 v[36:37], 0
	v_mov_b64_e32 v[38:39], 0
	v_mov_b64_e32 v[40:41], 0
	v_mov_b64_e32 v[42:43], 0
	v_mov_b64_e32 v[44:45], 0
	v_mov_b64_e32 v[46:47], 0
	v_mov_b64_e32 v[48:49], 0
	v_mov_b64_e32 v[50:51], 0
	v_mov_b64_e32 v[52:53], 0
	v_mov_b64_e32 v[54:55], 0
	v_mov_b64_e32 v[56:57], 0
	v_mov_b64_e32 v[58:59], 0
	v_mov_b64_e32 v[60:61], 0
	v_mov_b64_e32 v[62:63], 0
	v_mov_b64_e32 v[64:65], 0
	v_mov_b64_e32 v[66:67], 0
	v_mov_b64_e32 v[68:69], 0
	v_mov_b64_e32 v[70:71], 0
	v_mov_b64_e32 v[72:73], 0
	v_mov_b64_e32 v[74:75], 0
	v_mov_b64_e32 v[76:77], 0
	v_mov_b64_e32 v[78:79], 0
	v_mov_b64_e32 v[80:81], 0
	v_mov_b64_e32 v[82:83], 0
	v_mov_b64_e32 v[84:85], 0
	v_mov_b64_e32 v[86:87], 0
	v_mov_b64_e32 v[96:97], 0
	v_mov_b64_e32 v[98:99], 0
	v_mov_b64_e32 v[100:101], 0
	v_mov_b64_e32 v[102:103], 0
	v_mov_b64_e32 v[112:113], 0
	v_mov_b64_e32 v[114:115], 0
	v_mov_b64_e32 v[116:117], 0
	v_mov_b64_e32 v[118:119], 0
	s_cbranch_vccnz .LBB0_1135
	s_add_u32 s4, s28, s6
	s_addc_u32 s5, s29, s7
	s_add_u32 s60, s28, 0x100
	s_addc_u32 s61, s29, 0
	s_add_u32 s62, s26, 0x100
	s_addc_u32 s63, s27, 0
	s_add_u32 s4, s4, 0x80
	v_mov_b32_e32 v32, 0
	s_addc_u32 s5, s5, 0
	s_mov_b32 s26, 0
	v_mov_b64_e32 v[0:1], 0
	v_mov_b64_e32 v[2:3], 0
	v_mov_b64_e32 v[4:5], 0
	v_mov_b64_e32 v[6:7], 0
	v_mov_b64_e32 v[8:9], 0
	v_mov_b64_e32 v[10:11], 0
	v_mov_b64_e32 v[12:13], 0
	v_mov_b64_e32 v[14:15], 0
	v_mov_b64_e32 v[16:17], 0
	v_mov_b64_e32 v[18:19], 0
	v_mov_b64_e32 v[20:21], 0
	v_mov_b64_e32 v[22:23], 0
	v_mov_b64_e32 v[24:25], 0
	v_mov_b64_e32 v[26:27], 0
	v_mov_b64_e32 v[28:29], 0
	v_mov_b64_e32 v[30:31], 0
	v_mov_b64_e32 v[32:33], 0
	v_mov_b64_e32 v[34:35], 0
	v_mov_b64_e32 v[36:37], 0
	v_mov_b64_e32 v[38:39], 0
	v_mov_b64_e32 v[40:41], 0
	v_mov_b64_e32 v[42:43], 0
	v_mov_b64_e32 v[44:45], 0
	v_mov_b64_e32 v[46:47], 0
	v_mov_b64_e32 v[48:49], 0
	v_mov_b64_e32 v[50:51], 0
	v_mov_b64_e32 v[52:53], 0
	v_mov_b64_e32 v[54:55], 0
	v_mov_b64_e32 v[56:57], 0
	v_mov_b64_e32 v[58:59], 0
	v_mov_b64_e32 v[60:61], 0
	v_mov_b64_e32 v[62:63], 0
	v_mov_b64_e32 v[64:65], 0
	v_mov_b64_e32 v[66:67], 0
	v_mov_b64_e32 v[68:69], 0
	v_mov_b64_e32 v[70:71], 0
	v_mov_b64_e32 v[72:73], 0
	v_mov_b64_e32 v[74:75], 0
	v_mov_b64_e32 v[76:77], 0
	v_mov_b64_e32 v[78:79], 0
	v_mov_b64_e32 v[80:81], 0
	v_mov_b64_e32 v[82:83], 0
	v_mov_b64_e32 v[84:85], 0
	v_mov_b64_e32 v[86:87], 0
	v_mov_b64_e32 v[88:89], 0
	v_mov_b64_e32 v[90:91], 0
	v_mov_b64_e32 v[92:93], 0
	v_mov_b64_e32 v[94:95], 0
	v_mov_b64_e32 v[96:97], 0
	v_mov_b64_e32 v[98:99], 0
	v_mov_b64_e32 v[100:101], 0
	v_mov_b64_e32 v[102:103], 0
	v_mov_b64_e32 v[104:105], 0
	v_mov_b64_e32 v[106:107], 0
	v_mov_b64_e32 v[108:109], 0
	v_mov_b64_e32 v[110:111], 0
	v_mov_b64_e32 v[112:113], 0
	v_mov_b64_e32 v[114:115], 0
	v_mov_b64_e32 v[116:117], 0
	v_mov_b64_e32 v[118:119], 0
	v_mov_b64_e32 v[120:121], 0
	v_mov_b64_e32 v[122:123], 0
	v_mov_b64_e32 v[124:125], 0
	v_mov_b64_e32 v[126:127], 0

; template <class Epi, class Sched, bool ALIGN_EPI, bool FP8 = false>
; __device__ __forceinline__ void gemm_phase(PG8_LAS unsigned char* lds, const Gemm g, const Sched& S, const Epi& E, const int wid, const int lane) {
;     ...
;     f32x4 acc[2][2][4][2];
; #pragma unroll
;     for (int a = 0; a < 2; ++a)
; #pragma unroll
;         for (int b = 0; b < 2; ++b)
; #pragma unroll
;             for (int m = 0; m < 4; ++m)
; #pragma unroll
;                 for (int n = 0; n < 2; ++n) acc[a][b][m][n] = (f32x4){0.f, 0.f, 0.f, 0.f};
;     ...
; #pragma unroll
;         for (int a = 0; a < 2; ++a)
; #pragma unroll
;             for (int b = 0; b < 2; ++b)
; #pragma unroll
;                 for (int m = 0; m < 4; ++m)
; #pragma unroll
;                     for (int n = 0; n < 2; ++n) acc[a][b][m][n] = (f32x4){0.f, 0.f, 0.f, 0.f};
.LBB0_1452:
	v_mov_b32_e32 v35, 0
	s_andn2_b64 vcc, exec, s[14:15]
	v_mov_b64_e32 v[32:33], 0
	v_mov_b64_e32 v[34:35], 0
	v_mov_b64_e32 v[36:37], 0
	v_mov_b64_e32 v[38:39], 0
	v_mov_b64_e32 v[40:41], 0
	v_mov_b64_e32 v[42:43], 0
	v_mov_b64_e32 v[44:45], 0
	v_mov_b64_e32 v[46:47], 0
	v_mov_b64_e32 v[48:49], 0
	v_mov_b64_e32 v[50:51], 0
	v_mov_b64_e32 v[52:53], 0
	v_mov_b64_e32 v[54:55], 0
	v_mov_b64_e32 v[56:57], 0
	v_mov_b64_e32 v[58:59], 0
	v_mov_b64_e32 v[60:61], 0
	v_mov_b64_e32 v[62:63], 0
	v_mov_b64_e32 v[64:65], 0
	v_mov_b64_e32 v[66:67], 0
	v_mov_b64_e32 v[68:69], 0
	v_mov_b64_e32 v[70:71], 0
	v_mov_b64_e32 v[72:73], 0
	v_mov_b64_e32 v[74:75], 0
	v_mov_b64_e32 v[76:77], 0
	v_mov_b64_e32 v[78:79], 0
	v_mov_b64_e32 v[80:81], 0
	v_mov_b64_e32 v[82:83], 0
	v_mov_b64_e32 v[84:85], 0
	v_mov_b64_e32 v[86:87], 0
	v_mov_b64_e32 v[88:89], 0
	v_mov_b64_e32 v[90:91], 0
	v_mov_b64_e32 v[92:93], 0
	v_mov_b64_e32 v[94:95], 0
	v_mov_b64_e32 v[96:97], 0
	v_mov_b64_e32 v[98:99], 0
	v_mov_b64_e32 v[100:101], 0
	v_mov_b64_e32 v[102:103], 0
	v_mov_b64_e32 v[104:105], 0
	v_mov_b64_e32 v[106:107], 0
	v_mov_b64_e32 v[108:109], 0
	v_mov_b64_e32 v[110:111], 0
	v_mov_b64_e32 v[112:113], 0
	v_mov_b64_e32 v[114:115], 0
	v_mov_b64_e32 v[116:117], 0
	v_mov_b64_e32 v[118:119], 0
	v_mov_b64_e32 v[120:121], 0
	v_mov_b64_e32 v[122:123], 0
	v_mov_b64_e32 v[124:125], 0
	v_mov_b64_e32 v[126:127], 0
	v_mov_b64_e32 v[128:129], 0
	v_mov_b64_e32 v[130:131], 0
	v_mov_b64_e32 v[132:133], 0
	v_mov_b64_e32 v[134:135], 0
	v_mov_b64_e32 v[136:137], 0
	v_mov_b64_e32 v[138:139], 0
	v_mov_b64_e32 v[140:141], 0
	v_mov_b64_e32 v[142:143], 0
	v_mov_b64_e32 v[144:145], 0
	v_mov_b64_e32 v[146:147], 0
	v_mov_b64_e32 v[148:149], 0
	v_mov_b64_e32 v[150:151], 0
	v_mov_b64_e32 v[152:153], 0
	v_mov_b64_e32 v[154:155], 0
	v_mov_b64_e32 v[156:157], 0
	v_mov_b64_e32 v[158:159], 0
	s_cbranch_vccnz .LBB0_1455
	s_add_u32 s33, s30, s6
	s_addc_u32 s34, s31, s7
	s_add_u32 s84, s30, 0x100
	s_addc_u32 s85, s31, 0
	s_add_u32 s86, s28, 0x100
	s_addc_u32 s87, s29, 0
	s_add_u32 s28, s33, 0x80
	v_mov_b32_e32 v64, 0
	s_addc_u32 s29, s34, 0
	s_mov_b32 s30, 0
	v_mov_b64_e32 v[32:33], 0
	v_mov_b64_e32 v[34:35], 0
	v_mov_b64_e32 v[36:37], 0
	v_mov_b64_e32 v[38:39], 0
	v_mov_b64_e32 v[40:41], 0
	v_mov_b64_e32 v[42:43], 0
	v_mov_b64_e32 v[44:45], 0
	v_mov_b64_e32 v[46:47], 0
	v_mov_b64_e32 v[48:49], 0
	v_mov_b64_e32 v[50:51], 0
	v_mov_b64_e32 v[52:53], 0
	v_mov_b64_e32 v[54:55], 0
	v_mov_b64_e32 v[56:57], 0
	v_mov_b64_e32 v[58:59], 0
	v_mov_b64_e32 v[60:61], 0
	v_mov_b64_e32 v[62:63], 0
	v_mov_b64_e32 v[64:65], 0
	v_mov_b64_e32 v[66:67], 0
	v_mov_b64_e32 v[68:69], 0
	v_mov_b64_e32 v[70:71], 0
	v_mov_b64_e32 v[72:73], 0
	v_mov_b64_e32 v[74:75], 0
	v_mov_b64_e32 v[76:77], 0
	v_mov_b64_e32 v[78:79], 0
	v_mov_b64_e32 v[80:81], 0
	v_mov_b64_e32 v[82:83], 0
	v_mov_b64_e32 v[84:85], 0
	v_mov_b64_e32 v[86:87], 0
	v_mov_b64_e32 v[88:89], 0
	v_mov_b64_e32 v[90:91], 0
	v_mov_b64_e32 v[92:93], 0
	v_mov_b64_e32 v[94:95], 0
	v_mov_b64_e32 v[96:97], 0
	v_mov_b64_e32 v[98:99], 0
	v_mov_b64_e32 v[100:101], 0
	v_mov_b64_e32 v[102:103], 0
	v_mov_b64_e32 v[104:105], 0
	v_mov_b64_e32 v[106:107], 0
	v_mov_b64_e32 v[108:109], 0
	v_mov_b64_e32 v[110:111], 0
	v_mov_b64_e32 v[112:113], 0
	v_mov_b64_e32 v[114:115], 0
	v_mov_b64_e32 v[116:117], 0
	v_mov_b64_e32 v[118:119], 0
	v_mov_b64_e32 v[120:121], 0
	v_mov_b64_e32 v[122:123], 0
	v_mov_b64_e32 v[124:125], 0
	v_mov_b64_e32 v[126:127], 0
	v_mov_b64_e32 v[128:129], 0
	v_mov_b64_e32 v[130:131], 0
	v_mov_b64_e32 v[132:133], 0
	v_mov_b64_e32 v[134:135], 0
	v_mov_b64_e32 v[136:137], 0
	v_mov_b64_e32 v[138:139], 0
	v_mov_b64_e32 v[140:141], 0
	v_mov_b64_e32 v[142:143], 0
	v_mov_b64_e32 v[144:145], 0
	v_mov_b64_e32 v[146:147], 0
	v_mov_b64_e32 v[148:149], 0
	v_mov_b64_e32 v[150:151], 0
	v_mov_b64_e32 v[152:153], 0
	v_mov_b64_e32 v[154:155], 0
	v_mov_b64_e32 v[156:157], 0
	v_mov_b64_e32 v[158:159], 0

; template <class Epi, class Sched, bool ALIGN_EPI, bool FP8 = false>
; __device__ __forceinline__ void gemm_phase(PG8_LAS unsigned char* lds, const Gemm g, const Sched& S, const Epi& E, const int wid, const int lane) {
;     ...
; #pragma unroll
;         for (int a = 0; a < 2; ++a)
; #pragma unroll
;             for (int b = 0; b < 2; ++b)
; #pragma unroll
;                 for (int m = 0; m < 4; ++m)
; #pragma unroll
;                     for (int n = 0; n < 2; ++n) acc[a][b][m][n] = (f32x4){0.f, 0.f, 0.f, 0.f};
.LBB0_1636:
	v_mov_b32_e32 v68, 0
	s_mov_b32 s89, 0
	s_mov_b64 s[6:7], 0x100
	v_mov_b32_e32 v69, v68
	v_mov_b32_e32 v70, v68
	v_mov_b32_e32 v71, v68
	s_waitcnt vmcnt(0)
	v_mov_b64_e32 v[72:73], 0
	v_mov_b64_e32 v[74:75], 0
	v_mov_b64_e32 v[76:77], 0
	v_mov_b64_e32 v[78:79], 0
	v_mov_b64_e32 v[80:81], 0
	v_mov_b64_e32 v[82:83], 0
	v_mov_b64_e32 v[84:85], 0
	v_mov_b64_e32 v[86:87], 0
	v_mov_b64_e32 v[88:89], 0
	v_mov_b64_e32 v[90:91], 0
	v_mov_b64_e32 v[92:93], 0
	v_mov_b64_e32 v[94:95], 0
	v_mov_b64_e32 v[96:97], 0
	v_mov_b64_e32 v[98:99], 0
	v_mov_b64_e32 v[100:101], 0
	v_mov_b64_e32 v[102:103], 0
	v_mov_b64_e32 v[104:105], 0
	v_mov_b64_e32 v[106:107], 0
	v_mov_b64_e32 v[108:109], 0
	v_mov_b64_e32 v[110:111], 0
	v_mov_b64_e32 v[112:113], 0
	v_mov_b64_e32 v[114:115], 0
	v_mov_b64_e32 v[116:117], 0
	v_mov_b64_e32 v[118:119], 0
	v_mov_b64_e32 v[120:121], 0
	v_mov_b64_e32 v[122:123], 0
	v_mov_b64_e32 v[124:125], 0
	v_mov_b64_e32 v[126:127], 0
	v_mov_b64_e32 v[128:129], 0
	v_mov_b64_e32 v[130:131], 0
	v_mov_b64_e32 v[132:133], 0
	v_mov_b64_e32 v[134:135], 0
	v_mov_b64_e32 v[136:137], 0
	v_mov_b64_e32 v[138:139], 0
	v_mov_b64_e32 v[140:141], 0
	v_mov_b64_e32 v[142:143], 0
	v_mov_b64_e32 v[144:145], 0
	v_mov_b64_e32 v[146:147], 0
	v_mov_b64_e32 v[148:149], 0
	v_mov_b64_e32 v[150:151], 0
	v_mov_b64_e32 v[152:153], 0
	v_mov_b64_e32 v[154:155], 0
	v_mov_b64_e32 v[156:157], 0
	v_mov_b64_e32 v[158:159], 0
	v_mov_b64_e32 v[160:161], 0
	v_mov_b64_e32 v[162:163], 0
	v_mov_b64_e32 v[164:165], 0
	v_mov_b64_e32 v[166:167], 0
	v_mov_b64_e32 v[168:169], 0
	v_mov_b64_e32 v[170:171], 0
	v_mov_b64_e32 v[172:173], 0
	v_mov_b64_e32 v[174:175], 0
	v_mov_b64_e32 v[176:177], 0
	v_mov_b64_e32 v[178:179], 0
	v_mov_b64_e32 v[180:181], 0
	v_mov_b64_e32 v[182:183], 0
	v_mov_b64_e32 v[184:185], 0
	v_mov_b64_e32 v[186:187], 0
	v_mov_b64_e32 v[188:189], 0
	v_mov_b64_e32 v[190:191], 0
	v_mov_b64_e32 v[192:193], 0
	v_mov_b64_e32 v[194:195], 0
	s_branch .LBB0_1638

; template <class Epi, class Sched, bool ALIGN_EPI, bool FP8 = false>
; __device__ __forceinline__ void gemm_phase(PG8_LAS unsigned char* lds, const Gemm g, const Sched& S, const Epi& E, const int wid, const int lane) {
;     ...
; #pragma unroll
;         for (int a = 0; a < 2; ++a)
; #pragma unroll
;             for (int b = 0; b < 2; ++b)
; #pragma unroll
;                 for (int m = 0; m < 4; ++m)
; #pragma unroll
;                     for (int n = 0; n < 2; ++n) acc[a][b][m][n] = (f32x4){0.f, 0.f, 0.f, 0.f};
.LBB0_1658:
	v_mov_b64_e32 v[72:73], 0
	v_mov_b64_e32 v[74:75], 0
	v_mov_b64_e32 v[80:81], 0
	v_mov_b64_e32 v[82:83], 0
	v_mov_b64_e32 v[84:85], 0
	v_mov_b64_e32 v[86:87], 0
	v_mov_b64_e32 v[88:89], 0
	v_mov_b64_e32 v[90:91], 0
	v_mov_b64_e32 v[92:93], 0
	v_mov_b64_e32 v[94:95], 0
	v_mov_b64_e32 v[96:97], 0
	v_mov_b64_e32 v[98:99], 0
	v_mov_b64_e32 v[100:101], 0
	v_mov_b64_e32 v[102:103], 0
	v_mov_b64_e32 v[104:105], 0
	v_mov_b64_e32 v[106:107], 0
	v_mov_b64_e32 v[108:109], 0
	v_mov_b64_e32 v[110:111], 0
	v_mov_b64_e32 v[112:113], 0
	v_mov_b64_e32 v[114:115], 0
	v_mov_b64_e32 v[116:117], 0
	v_mov_b64_e32 v[118:119], 0
	v_mov_b64_e32 v[120:121], 0
	v_mov_b64_e32 v[122:123], 0
	v_mov_b64_e32 v[124:125], 0
	v_mov_b64_e32 v[126:127], 0
	v_mov_b64_e32 v[128:129], 0
	v_mov_b64_e32 v[130:131], 0
	v_mov_b64_e32 v[132:133], 0
	v_mov_b64_e32 v[134:135], 0
	v_mov_b64_e32 v[136:137], 0
	v_mov_b64_e32 v[138:139], 0
	v_mov_b64_e32 v[140:141], 0
	v_mov_b64_e32 v[142:143], 0
	v_mov_b64_e32 v[144:145], 0
	v_mov_b64_e32 v[146:147], 0
	v_mov_b64_e32 v[148:149], 0
	v_mov_b64_e32 v[150:151], 0
	v_mov_b64_e32 v[152:153], 0
	v_mov_b64_e32 v[154:155], 0
	v_mov_b64_e32 v[156:157], 0
	v_mov_b64_e32 v[158:159], 0
	v_mov_b64_e32 v[160:161], 0
	v_mov_b64_e32 v[162:163], 0
	v_mov_b64_e32 v[164:165], 0
	v_mov_b64_e32 v[166:167], 0
	v_mov_b64_e32 v[168:169], 0
	v_mov_b64_e32 v[170:171], 0
	v_mov_b64_e32 v[172:173], 0
	v_mov_b64_e32 v[174:175], 0
	v_mov_b64_e32 v[176:177], 0
	v_mov_b64_e32 v[178:179], 0
	v_mov_b64_e32 v[180:181], 0
	v_mov_b64_e32 v[182:183], 0
	v_mov_b64_e32 v[184:185], 0
	v_mov_b64_e32 v[186:187], 0
	v_mov_b64_e32 v[188:189], 0
	v_mov_b64_e32 v[190:191], 0
	v_mov_b64_e32 v[192:193], 0
	v_mov_b64_e32 v[194:195], 0
	s_waitcnt vmcnt(0)
	v_mov_b32_e32 v79, v195
	v_mov_b32_e32 v78, v195
	v_mov_b32_e32 v77, v195
	v_mov_b32_e32 v76, v195
	v_mov_b32_e32 v71, v195
	v_mov_b32_e32 v70, v195
	v_mov_b32_e32 v69, v195
	v_mov_b32_e32 v68, v195

; template <class Epi, class Sched, bool ALIGN_EPI, bool FP8 = false>
; __device__ __forceinline__ void gemm_phase(PG8_LAS unsigned char* lds, const Gemm g, const Sched& S, const Epi& E, const int wid, const int lane) {
;     ...
; #pragma unroll
;         for (int a = 0; a < 2; ++a)
; #pragma unroll
;             for (int b = 0; b < 2; ++b)
; #pragma unroll
;                 for (int m = 0; m < 4; ++m)
; #pragma unroll
;                     for (int n = 0; n < 2; ++n) acc[a][b][m][n] = (f32x4){0.f, 0.f, 0.f, 0.f};
;         cur = nxt; cA = nA; cB = nB; ++ui;
.LBB0_1760:
	s_waitcnt vmcnt(9)
	v_mov_b32_e32 v35, 0
	s_andn2_b64 vcc, exec, s[22:23]
	v_mov_b32_e32 v34, v35
	v_mov_b32_e32 v33, v35
	v_mov_b32_e32 v32, v35
	s_waitcnt vmcnt(8)
	v_mov_b32_e32 v39, v35
	v_mov_b32_e32 v38, v35
	v_mov_b32_e32 v37, v35
	v_mov_b32_e32 v36, v35
	s_waitcnt vmcnt(5)
	v_mov_b32_e32 v51, v35
	v_mov_b32_e32 v50, v35
	v_mov_b32_e32 v49, v35
	v_mov_b32_e32 v48, v35
	s_waitcnt vmcnt(4)
	v_mov_b64_e32 v[52:53], 0
	v_mov_b64_e32 v[54:55], 0
	v_mov_b64_e32 v[88:89], 0
	v_mov_b64_e32 v[90:91], 0
	v_mov_b64_e32 v[92:93], 0
	v_mov_b64_e32 v[94:95], 0
	v_mov_b64_e32 v[96:97], 0
	v_mov_b64_e32 v[98:99], 0
	v_mov_b64_e32 v[100:101], 0
	v_mov_b64_e32 v[102:103], 0
	v_mov_b64_e32 v[104:105], 0
	v_mov_b64_e32 v[106:107], 0
	v_mov_b64_e32 v[108:109], 0
	v_mov_b64_e32 v[110:111], 0
	v_mov_b64_e32 v[112:113], 0
	v_mov_b64_e32 v[114:115], 0
	v_mov_b64_e32 v[116:117], 0
	v_mov_b64_e32 v[118:119], 0
	v_mov_b64_e32 v[120:121], 0
	v_mov_b64_e32 v[122:123], 0
	v_mov_b64_e32 v[124:125], 0
	v_mov_b64_e32 v[126:127], 0
	v_mov_b64_e32 v[128:129], 0
	v_mov_b64_e32 v[130:131], 0
	v_mov_b64_e32 v[132:133], 0
	v_mov_b64_e32 v[134:135], 0
	v_mov_b64_e32 v[136:137], 0
	v_mov_b64_e32 v[138:139], 0
	v_mov_b64_e32 v[140:141], 0
	v_mov_b64_e32 v[142:143], 0
	v_mov_b64_e32 v[144:145], 0
	v_mov_b64_e32 v[146:147], 0
	v_mov_b64_e32 v[148:149], 0
	v_mov_b64_e32 v[150:151], 0
	v_mov_b64_e32 v[152:153], 0
	v_mov_b64_e32 v[154:155], 0
	v_mov_b64_e32 v[156:157], 0
	v_mov_b64_e32 v[158:159], 0
	s_waitcnt vmcnt(0)
	v_mov_b32_e32 v79, v35
	v_mov_b32_e32 v78, v35
	v_mov_b32_e32 v77, v35
	v_mov_b32_e32 v76, v35
	v_mov_b32_e32 v75, v35
	v_mov_b32_e32 v74, v35
	v_mov_b32_e32 v73, v35
	v_mov_b32_e32 v72, v35
	v_mov_b32_e32 v63, v35
	v_mov_b32_e32 v62, v35
	v_mov_b32_e32 v61, v35
	v_mov_b32_e32 v60, v35
	v_mov_b32_e32 v59, v35
	v_mov_b32_e32 v58, v35
	v_mov_b32_e32 v57, v35
	v_mov_b32_e32 v56, v35
	v_mov_b32_e32 v47, v35
	v_mov_b32_e32 v46, v35
	v_mov_b32_e32 v45, v35
	v_mov_b32_e32 v44, v35
	v_mov_b32_e32 v43, v35
	v_mov_b32_e32 v42, v35
	v_mov_b32_e32 v41, v35
	v_mov_b32_e32 v40, v35
	v_mov_b32_e32 v87, v35
	v_mov_b32_e32 v86, v35
	v_mov_b32_e32 v85, v35
	v_mov_b32_e32 v84, v35
	v_mov_b32_e32 v83, v35
	v_mov_b32_e32 v82, v35
	v_mov_b32_e32 v81, v35
	v_mov_b32_e32 v80, v35
	v_mov_b32_e32 v71, v35
	v_mov_b32_e32 v70, v35
	v_mov_b32_e32 v69, v35
	v_mov_b32_e32 v68, v35
	v_mov_b32_e32 v67, v35
	v_mov_b32_e32 v66, v35
	v_mov_b32_e32 v65, v35
	v_mov_b32_e32 v64, v35
	s_cbranch_vccnz .LBB0_1763
	s_add_u32 s33, s8, s12
	s_addc_u32 s34, s9, s13
	s_add_u32 s75, s8, 0x100
	s_addc_u32 s80, s9, 0
	s_add_u32 s81, s6, 0x100
	s_addc_u32 s82, s7, 0
	s_add_u32 s6, s33, 0x80
	v_mov_b32_e32 v64, 0
	s_addc_u32 s7, s34, 0
	s_mov_b32 s8, 0
	v_mov_b64_e32 v[32:33], 0
	v_mov_b64_e32 v[34:35], 0
	v_mov_b64_e32 v[36:37], 0
	v_mov_b64_e32 v[38:39], 0
	v_mov_b64_e32 v[40:41], 0
	v_mov_b64_e32 v[42:43], 0
	v_mov_b64_e32 v[44:45], 0
	v_mov_b64_e32 v[46:47], 0
	v_mov_b64_e32 v[48:49], 0
	v_mov_b64_e32 v[50:51], 0
	v_mov_b64_e32 v[52:53], 0
	v_mov_b64_e32 v[54:55], 0
	v_mov_b64_e32 v[56:57], 0
	v_mov_b64_e32 v[58:59], 0
	v_mov_b64_e32 v[60:61], 0
	v_mov_b64_e32 v[62:63], 0
	v_mov_b64_e32 v[64:65], 0
	v_mov_b64_e32 v[66:67], 0
	v_mov_b64_e32 v[68:69], 0
	v_mov_b64_e32 v[70:71], 0
	v_mov_b64_e32 v[72:73], 0
	v_mov_b64_e32 v[74:75], 0
	v_mov_b64_e32 v[76:77], 0
	v_mov_b64_e32 v[78:79], 0
	v_mov_b64_e32 v[80:81], 0
	v_mov_b64_e32 v[82:83], 0
	v_mov_b64_e32 v[84:85], 0
	v_mov_b64_e32 v[86:87], 0
	v_mov_b64_e32 v[88:89], 0
	v_mov_b64_e32 v[90:91], 0
	v_mov_b64_e32 v[92:93], 0
	v_mov_b64_e32 v[94:95], 0
	v_mov_b64_e32 v[96:97], 0
	v_mov_b64_e32 v[98:99], 0
	v_mov_b64_e32 v[100:101], 0
	v_mov_b64_e32 v[102:103], 0
	v_mov_b64_e32 v[104:105], 0
	v_mov_b64_e32 v[106:107], 0
	v_mov_b64_e32 v[108:109], 0
	v_mov_b64_e32 v[110:111], 0
	v_mov_b64_e32 v[112:113], 0
	v_mov_b64_e32 v[114:115], 0
	v_mov_b64_e32 v[116:117], 0
	v_mov_b64_e32 v[118:119], 0
	v_mov_b64_e32 v[120:121], 0
	v_mov_b64_e32 v[122:123], 0
	v_mov_b64_e32 v[124:125], 0
	v_mov_b64_e32 v[126:127], 0
	v_mov_b64_e32 v[128:129], 0
	v_mov_b64_e32 v[130:131], 0
	v_mov_b64_e32 v[132:133], 0
	v_mov_b64_e32 v[134:135], 0
	v_mov_b64_e32 v[136:137], 0
	v_mov_b64_e32 v[138:139], 0
	v_mov_b64_e32 v[140:141], 0
	v_mov_b64_e32 v[142:143], 0
	v_mov_b64_e32 v[144:145], 0
	v_mov_b64_e32 v[146:147], 0
	v_mov_b64_e32 v[148:149], 0
	v_mov_b64_e32 v[150:151], 0
	v_mov_b64_e32 v[152:153], 0
	v_mov_b64_e32 v[154:155], 0
	v_mov_b64_e32 v[156:157], 0
	v_mov_b64_e32 v[158:159], 0
